# v26: v25 + mix_norm_gate hot loop: same restructuring (table loads of 4 column blocks issued together into the prefetch registers, prefetch after the table section)
# speedup vs baseline: 1.0224x; 1.0050x over previous
.LBB0_152:
	s_or_b64 exec, exec, s[4:5]
	s_waitcnt vmcnt(0)
	s_add_i32 s0, s0, 2
	s_add_i32 s12, s12, s33
	v_mov_b64_e32 v[130:131], v[126:127]
	v_mov_b64_e32 v[138:139], v[122:123]
	v_mov_b64_e32 v[146:147], v[118:119]
	v_mov_b64_e32 v[154:155], v[114:115]
	v_mov_b64_e32 v[162:163], v[110:111]
	v_mov_b64_e32 v[170:171], v[106:107]
	v_mov_b64_e32 v[178:179], v[102:103]
	v_mov_b64_e32 v[186:187], v[98:99]
	v_mov_b64_e32 v[134:135], v[94:95]
	v_mov_b64_e32 v[142:143], v[90:91]
	v_mov_b64_e32 v[150:151], v[86:87]
	v_mov_b64_e32 v[158:159], v[82:83]
	v_mov_b64_e32 v[166:167], v[78:79]
	v_mov_b64_e32 v[174:175], v[74:75]
	v_mov_b64_e32 v[182:183], v[70:71]
	v_mov_b64_e32 v[190:191], v[66:67]
	s_cmp_eq_u32 s44, s41
	v_mov_b64_e32 v[128:129], v[124:125]
	v_mov_b64_e32 v[136:137], v[120:121]
	v_mov_b64_e32 v[144:145], v[116:117]
	v_mov_b64_e32 v[152:153], v[112:113]
	v_mov_b64_e32 v[160:161], v[108:109]
	v_mov_b64_e32 v[168:169], v[104:105]
	v_mov_b64_e32 v[176:177], v[100:101]
	v_mov_b64_e32 v[184:185], v[96:97]
	v_mov_b64_e32 v[132:133], v[92:93]
	v_mov_b64_e32 v[140:141], v[88:89]
	v_mov_b64_e32 v[148:149], v[84:85]
	v_mov_b64_e32 v[156:157], v[80:81]
	v_mov_b64_e32 v[164:165], v[76:77]
	v_mov_b64_e32 v[172:173], v[72:73]
	v_mov_b64_e32 v[180:181], v[68:69]
	v_mov_b64_e32 v[188:189], v[64:65]
	s_cbranch_scc1 .LBB0_159

.LBB0_155:
	s_waitcnt vmcnt(15)
	v_mov_b64_e32 v[124:125], v[128:129]
	s_waitcnt vmcnt(14)
	v_mov_b64_e32 v[120:121], v[136:137]
	s_waitcnt vmcnt(13)
	v_mov_b64_e32 v[116:117], v[144:145]
	s_waitcnt vmcnt(12)
	v_mov_b64_e32 v[112:113], v[152:153]
	s_waitcnt vmcnt(11)
	v_mov_b64_e32 v[108:109], v[160:161]
	s_waitcnt vmcnt(10)
	v_mov_b64_e32 v[104:105], v[168:169]
	s_waitcnt vmcnt(9)
	v_mov_b64_e32 v[100:101], v[176:177]
	s_waitcnt vmcnt(8)
	v_mov_b64_e32 v[96:97], v[184:185]
	s_waitcnt vmcnt(7)
	v_mov_b64_e32 v[92:93], v[132:133]
	s_waitcnt vmcnt(6)
	v_mov_b64_e32 v[88:89], v[140:141]
	s_waitcnt vmcnt(5)
	v_mov_b64_e32 v[84:85], v[148:149]
	s_waitcnt vmcnt(4)
	v_mov_b64_e32 v[80:81], v[156:157]
	s_waitcnt vmcnt(3)
	v_mov_b64_e32 v[76:77], v[164:165]
	s_waitcnt vmcnt(2)
	v_mov_b64_e32 v[72:73], v[172:173]
	s_waitcnt vmcnt(1)
	v_mov_b64_e32 v[68:69], v[180:181]
	s_waitcnt vmcnt(0)
	v_mov_b64_e32 v[64:65], v[188:189]
	s_andn2_b64 vcc, exec, s[4:5]
	v_mov_b64_e32 v[126:127], v[130:131]
	v_mov_b64_e32 v[122:123], v[138:139]
	v_mov_b64_e32 v[118:119], v[146:147]
	v_mov_b64_e32 v[114:115], v[154:155]
	v_mov_b64_e32 v[110:111], v[162:163]
	v_mov_b64_e32 v[106:107], v[170:171]
	v_mov_b64_e32 v[102:103], v[178:179]
	v_mov_b64_e32 v[98:99], v[186:187]
	v_mov_b64_e32 v[94:95], v[134:135]
	v_mov_b64_e32 v[90:91], v[142:143]
	v_mov_b64_e32 v[86:87], v[150:151]
	v_mov_b64_e32 v[82:83], v[158:159]
	v_mov_b64_e32 v[78:79], v[166:167]
	v_mov_b64_e32 v[74:75], v[174:175]
	v_mov_b64_e32 v[70:71], v[182:183]
	v_mov_b64_e32 v[66:67], v[190:191]
	v_ashrrev_i32_e32 v215, 31, v214
	v_ashrrev_i32_e32 v213, 31, v212
	v_ashrrev_i32_e32 v211, 31, v210
	v_ashrrev_i32_e32 v209, 31, v208
	v_ashrrev_i32_e32 v221, 31, v220
	v_ashrrev_i32_e32 v219, 31, v218
	v_ashrrev_i32_e32 v217, 31, v216
.LBB0_157:
	v_mul_f32_e32 v192, v189, v189
	v_mul_f32_e32 v193, v181, v181
	v_fmac_f32_e32 v192, v188, v188
	v_fmac_f32_e32 v193, v180, v180
	v_fmac_f32_e32 v192, v190, v190
	v_fmac_f32_e32 v193, v182, v182
	v_fmac_f32_e32 v192, v191, v191
	v_fmac_f32_e32 v193, v183, v183
	v_mov_b32_e32 v194, v165
	v_mov_b32_e32 v195, v173
	v_add_f32_e32 v196, v193, v192
	v_mov_b32_e32 v192, v164
	v_mov_b32_e32 v193, v172
	v_pk_mul_f32 v[194:195], v[194:195], v[194:195]
	s_nop 0
	v_pk_fma_f32 v[192:193], v[192:193], v[192:193], v[194:195]
	v_mov_b32_e32 v194, v166
	v_mov_b32_e32 v195, v174
	v_pk_fma_f32 v[192:193], v[194:195], v[194:195], v[192:193]
	v_mov_b32_e32 v194, v167
	v_mov_b32_e32 v195, v175
	v_pk_fma_f32 v[192:193], v[194:195], v[194:195], v[192:193]
	v_mov_b32_e32 v194, v149
	v_add_f32_e32 v193, v193, v196
	v_mov_b32_e32 v195, v157
	v_add_f32_e32 v196, v192, v193
	v_mov_b32_e32 v192, v148
	v_mov_b32_e32 v193, v156
	v_pk_mul_f32 v[194:195], v[194:195], v[194:195]
	s_nop 0
	v_pk_fma_f32 v[192:193], v[192:193], v[192:193], v[194:195]
	v_mov_b32_e32 v194, v150
	v_mov_b32_e32 v195, v158
	v_pk_fma_f32 v[192:193], v[194:195], v[194:195], v[192:193]
	v_mov_b32_e32 v194, v151
	v_mov_b32_e32 v195, v159
	v_pk_fma_f32 v[192:193], v[194:195], v[194:195], v[192:193]
	v_mov_b32_e32 v194, v133
	v_add_f32_e32 v193, v193, v196
	v_mov_b32_e32 v195, v141
	v_add_f32_e32 v196, v192, v193
	v_mov_b32_e32 v192, v132
	v_mov_b32_e32 v193, v140
	v_pk_mul_f32 v[194:195], v[194:195], v[194:195]
	s_nop 0
	v_pk_fma_f32 v[192:193], v[192:193], v[192:193], v[194:195]
	v_mov_b32_e32 v194, v134
	v_mov_b32_e32 v195, v142
	v_pk_fma_f32 v[192:193], v[194:195], v[194:195], v[192:193]
	v_mov_b32_e32 v194, v135
	v_mov_b32_e32 v195, v143
	v_pk_fma_f32 v[192:193], v[194:195], v[194:195], v[192:193]
	s_nop 0
	v_add_f32_e32 v193, v193, v196
	v_add_f32_e32 v192, v192, v193
	s_nop 1
	v_add_f32_dpp v192, v192, v192 quad_perm:[1,0,3,2] row_mask:0xf bank_mask:0xf bound_ctrl:1
	s_nop 1
	v_add_f32_dpp v192, v192, v192 quad_perm:[2,3,0,1] row_mask:0xf bank_mask:0xf bound_ctrl:1
	s_nop 1
	v_add_f32_dpp v192, v192, v192 row_half_mirror row_mask:0xf bank_mask:0xf bound_ctrl:1
	s_nop 1
	v_add_f32_dpp v192, v192, v192 row_mirror row_mask:0xf bank_mask:0xf bound_ctrl:1
	s_nop 0
	v_readlane_b32 s13, v192, 16
	v_readlane_b32 s16, v192, 48
	v_readlane_b32 s4, v192, 0
	v_readlane_b32 s5, v192, 32
	v_mov_b32_e32 v192, s13
	v_mov_b32_e32 v193, s16
	v_pk_add_f32 v[192:193], s[4:5], v[192:193]
	s_nop 0
	v_add_f32_e32 v192, v192, v193
	v_fmamk_f32 v192, v192, 0x3a000000, v241
	v_cmp_gt_f32_e32 vcc, s34, v192
	v_mul_f32_e32 v193, 0x4f800000, v192
	s_nop 0
	v_cndmask_b32_e32 v192, v192, v193, vcc
	v_sqrt_f32_e32 v193, v192
	s_nop 0
	v_add_u32_e32 v194, -1, v193
	v_fma_f32 v195, -v194, v193, v192
	v_cmp_ge_f32_e64 s[4:5], 0, v195
	v_add_u32_e32 v195, 1, v193
	s_nop 0
	v_cndmask_b32_e64 v194, v193, v194, s[4:5]
	v_fma_f32 v193, -v195, v193, v192
	v_cmp_lt_f32_e64 s[4:5], 0, v193
	s_nop 1
	v_cndmask_b32_e64 v193, v194, v195, s[4:5]
	v_mul_f32_e32 v194, 0x37800000, v193
	v_cndmask_b32_e32 v193, v193, v194, vcc
	v_cmp_class_f32_e32 vcc, v192, v242
	s_nop 1
	v_cndmask_b32_e32 v192, v193, v192, vcc
	v_div_scale_f32 v193, s[4:5], v192, v192, 1.0
	v_rcp_f32_e32 v194, v193
	s_nop 0
	v_fma_f32 v195, -v193, v194, 1.0
	v_fmac_f32_e32 v194, v195, v194
	v_div_scale_f32 v195, vcc, 1.0, v192, 1.0
	v_mul_f32_e32 v196, v195, v194
	v_fma_f32 v197, -v193, v196, v195
	v_fmac_f32_e32 v196, v197, v194
	v_fma_f32 v193, -v193, v196, v195
	v_div_fmas_f32 v193, v193, v194, v196
	v_div_fixup_f32 v204, v193, v192, 1.0
	v_mul_f32_e32 v192, v185, v185
	v_mul_f32_e32 v193, v177, v177
	v_fmac_f32_e32 v192, v184, v184
	v_fmac_f32_e32 v193, v176, v176
	v_fmac_f32_e32 v192, v186, v186
	v_fmac_f32_e32 v193, v178, v178
	v_fmac_f32_e32 v192, v187, v187
	v_fmac_f32_e32 v193, v179, v179
	v_mov_b32_e32 v194, v161
	v_mov_b32_e32 v195, v169
	v_add_f32_e32 v196, v193, v192
	v_mov_b32_e32 v192, v160
	v_mov_b32_e32 v193, v168
	v_pk_mul_f32 v[194:195], v[194:195], v[194:195]
	s_nop 0
	v_pk_fma_f32 v[192:193], v[192:193], v[192:193], v[194:195]
	v_mov_b32_e32 v194, v162
	v_mov_b32_e32 v195, v170
	v_pk_fma_f32 v[192:193], v[194:195], v[194:195], v[192:193]
	v_mov_b32_e32 v194, v163
	v_mov_b32_e32 v195, v171
	v_pk_fma_f32 v[192:193], v[194:195], v[194:195], v[192:193]
	v_mov_b32_e32 v194, v145
	v_add_f32_e32 v193, v193, v196
	v_mov_b32_e32 v195, v153
	v_add_f32_e32 v196, v192, v193
	v_mov_b32_e32 v192, v144
	v_mov_b32_e32 v193, v152
	v_pk_mul_f32 v[194:195], v[194:195], v[194:195]
	s_nop 0
	v_pk_fma_f32 v[192:193], v[192:193], v[192:193], v[194:195]
	v_mov_b32_e32 v194, v146
	v_mov_b32_e32 v195, v154
	v_pk_fma_f32 v[192:193], v[194:195], v[194:195], v[192:193]
	v_mov_b32_e32 v194, v147
	v_mov_b32_e32 v195, v155
	v_pk_fma_f32 v[192:193], v[194:195], v[194:195], v[192:193]
	v_mov_b32_e32 v194, v129
	v_add_f32_e32 v193, v193, v196
	v_mov_b32_e32 v195, v137
	v_add_f32_e32 v196, v192, v193
	v_mov_b32_e32 v192, v128
	v_mov_b32_e32 v193, v136
	v_pk_mul_f32 v[194:195], v[194:195], v[194:195]
	s_nop 0
	v_pk_fma_f32 v[192:193], v[192:193], v[192:193], v[194:195]
	v_mov_b32_e32 v194, v130
	v_mov_b32_e32 v195, v138
	v_pk_fma_f32 v[192:193], v[194:195], v[194:195], v[192:193]
	v_mov_b32_e32 v194, v131
	v_mov_b32_e32 v195, v139
	v_pk_fma_f32 v[192:193], v[194:195], v[194:195], v[192:193]
	s_nop 0
	v_add_f32_e32 v193, v193, v196
	v_add_f32_e32 v192, v192, v193
	s_nop 1
	v_add_f32_dpp v192, v192, v192 quad_perm:[1,0,3,2] row_mask:0xf bank_mask:0xf bound_ctrl:1
	s_nop 1
	v_add_f32_dpp v192, v192, v192 quad_perm:[2,3,0,1] row_mask:0xf bank_mask:0xf bound_ctrl:1
	s_nop 1
	v_add_f32_dpp v192, v192, v192 row_half_mirror row_mask:0xf bank_mask:0xf bound_ctrl:1
	s_nop 1
	v_add_f32_dpp v192, v192, v192 row_mirror row_mask:0xf bank_mask:0xf bound_ctrl:1
	s_nop 0
	v_readlane_b32 s13, v192, 16
	v_readlane_b32 s16, v192, 48
	v_readlane_b32 s4, v192, 0
	v_readlane_b32 s5, v192, 32
	v_mov_b32_e32 v192, s13
	v_mov_b32_e32 v193, s16
	v_pk_add_f32 v[192:193], s[4:5], v[192:193]
	s_nop 0
	v_add_f32_e32 v192, v192, v193
	v_fmamk_f32 v192, v192, 0x3a000000, v241
	v_cmp_gt_f32_e32 vcc, s34, v192
	v_mul_f32_e32 v193, 0x4f800000, v192
	s_nop 0
	v_cndmask_b32_e32 v192, v192, v193, vcc
	v_sqrt_f32_e32 v193, v192
	s_nop 0
	v_add_u32_e32 v194, -1, v193
	v_fma_f32 v195, -v194, v193, v192
	v_cmp_ge_f32_e64 s[4:5], 0, v195
	v_add_u32_e32 v195, 1, v193
	s_nop 0
	v_cndmask_b32_e64 v194, v193, v194, s[4:5]
	v_fma_f32 v193, -v195, v193, v192
	v_cmp_lt_f32_e64 s[4:5], 0, v193
	s_nop 1
	v_cndmask_b32_e64 v193, v194, v195, s[4:5]
	v_mul_f32_e32 v194, 0x37800000, v193
	v_cndmask_b32_e32 v193, v193, v194, vcc
	v_cmp_class_f32_e32 vcc, v192, v242
	s_nop 1
	v_cndmask_b32_e32 v192, v193, v192, vcc
	v_div_scale_f32 v193, s[4:5], v192, v192, 1.0
	v_rcp_f32_e32 v194, v193
	s_ashr_i32 s4, s12, 12
	s_mul_hi_i32 s5, s4, 0xc000
	s_mul_i32 s4, s4, 0xc000
	v_fma_f32 v195, -v193, v194, 1.0
	v_fmac_f32_e32 v194, v195, v194
	v_div_scale_f32 v195, vcc, 1.0, v192, 1.0
	v_mul_f32_e32 v196, v195, v194
	v_fma_f32 v197, -v193, v196, v195
	s_add_u32 s16, s25, s4
	v_fmac_f32_e32 v196, v197, v194
	s_addc_u32 s17, s26, s5
	s_ashr_i32 s13, s12, 31
	v_fma_f32 v193, -v193, v196, v195
	s_lshl_b64 s[4:5], s[12:13], 12
	v_div_fmas_f32 v193, v193, v194, v196
	s_add_u32 s4, s1, s4
	v_div_fixup_f32 v224, v193, v192, 1.0
	s_addc_u32 s5, s20, s5
	v_lshlrev_b64 v[192:193], 1, v[222:223]
	v_lshl_add_u64 v[194:195], s[4:5], 0, v[192:193]
	v_cvt_pk_bf16_f32 v196, v188, v189
	v_cvt_pk_bf16_f32 v197, v190, v191
	global_store_dwordx2 v[194:195], v[196:197], off
	v_lshlrev_b64 v[194:195], 1, v[220:221]
	v_lshl_add_u64 v[196:197], s[4:5], 0, v[194:195]
	v_cvt_pk_bf16_f32 v198, v180, v181
	v_cvt_pk_bf16_f32 v199, v182, v183
	global_store_dwordx2 v[196:197], v[198:199], off
	v_lshlrev_b64 v[196:197], 1, v[218:219]
	v_lshl_add_u64 v[198:199], s[4:5], 0, v[196:197]
	v_cvt_pk_bf16_f32 v200, v172, v173
	v_cvt_pk_bf16_f32 v201, v174, v175
	global_store_dwordx2 v[198:199], v[200:201], off
	v_lshlrev_b64 v[198:199], 1, v[216:217]
	v_lshl_add_u64 v[200:201], s[4:5], 0, v[198:199]
	v_cvt_pk_bf16_f32 v202, v164, v165
	v_cvt_pk_bf16_f32 v203, v166, v167
	global_store_dwordx2 v[200:201], v[202:203], off
	v_lshlrev_b64 v[200:201], 1, v[214:215]
	v_lshl_add_u64 v[202:203], s[4:5], 0, v[200:201]
	v_cvt_pk_bf16_f32 v248, v156, v157
	v_cvt_pk_bf16_f32 v249, v158, v159
	global_store_dwordx2 v[202:203], v[248:249], off
	v_lshlrev_b64 v[202:203], 1, v[212:213]
	v_lshl_add_u64 v[248:249], s[4:5], 0, v[202:203]
	v_cvt_pk_bf16_f32 v250, v148, v149
	v_cvt_pk_bf16_f32 v251, v150, v151
	global_store_dwordx2 v[248:249], v[250:251], off
	v_lshlrev_b64 v[248:249], 1, v[210:211]
	v_lshl_add_u64 v[250:251], s[4:5], 0, v[248:249]
	v_cvt_pk_bf16_f32 v244, v140, v141
	v_cvt_pk_bf16_f32 v245, v142, v143
	global_store_dwordx2 v[250:251], v[244:245], off
	v_lshlrev_b64 v[244:245], 1, v[208:209]
	v_lshl_add_u64 v[250:251], s[4:5], 0, v[244:245]
	s_add_i32 s4, s21, s12
	s_ashr_i32 s5, s4, 31
	s_lshl_b64 s[18:19], s[4:5], 12
	s_add_u32 s18, s1, s18
	s_addc_u32 s19, s20, s19
	v_cvt_pk_bf16_f32 v246, v132, v133
	v_cvt_pk_bf16_f32 v247, v134, v135
	v_lshl_add_u64 v[192:193], s[18:19], 0, v[192:193]
	global_store_dwordx2 v[250:251], v[246:247], off
	v_cvt_pk_bf16_f32 v246, v184, v185
	v_cvt_pk_bf16_f32 v247, v186, v187
	global_store_dwordx2 v[192:193], v[246:247], off
	v_lshl_add_u64 v[192:193], s[18:19], 0, v[194:195]
	v_cvt_pk_bf16_f32 v194, v176, v177
	v_cvt_pk_bf16_f32 v195, v178, v179
	global_store_dwordx2 v[192:193], v[194:195], off
	v_lshl_add_u64 v[192:193], s[18:19], 0, v[196:197]
	v_cvt_pk_bf16_f32 v194, v168, v169
	v_cvt_pk_bf16_f32 v195, v170, v171
	global_store_dwordx2 v[192:193], v[194:195], off
	v_lshl_add_u64 v[192:193], s[18:19], 0, v[198:199]
	v_cvt_pk_bf16_f32 v194, v160, v161
	v_cvt_pk_bf16_f32 v195, v162, v163
	global_store_dwordx2 v[192:193], v[194:195], off
	v_lshl_add_u64 v[192:193], s[18:19], 0, v[200:201]
	v_cvt_pk_bf16_f32 v194, v152, v153
	v_cvt_pk_bf16_f32 v195, v154, v155
	global_store_dwordx2 v[192:193], v[194:195], off
	v_lshl_add_u64 v[192:193], s[18:19], 0, v[202:203]
	v_cvt_pk_bf16_f32 v194, v144, v145
	v_cvt_pk_bf16_f32 v195, v146, v147
	global_store_dwordx2 v[192:193], v[194:195], off
	v_lshl_add_u64 v[192:193], s[18:19], 0, v[248:249]
	v_cvt_pk_bf16_f32 v194, v136, v137
	v_cvt_pk_bf16_f32 v195, v138, v139
	global_store_dwordx2 v[192:193], v[194:195], off
	v_lshl_add_u64 v[192:193], s[18:19], 0, v[244:245]
	s_add_u32 s18, s16, 0x2000
	v_cvt_pk_bf16_f32 v194, v128, v129
	v_cvt_pk_bf16_f32 v195, v130, v131
	global_store_dwordx2 v[192:193], v[194:195], off
	s_addc_u32 s19, s17, 0
	v_lshlrev_b32_e32 v192, 3, v226
	v_lshlrev_b64 v[196:197], 2, v[222:223]
	v_and_b32_e32 v207, 8, v192
	v_lshl_add_u64 v[192:193], s[8:9], 0, v[196:197]
	v_lshl_add_u64 v[198:199], s[18:19], 0, v[196:197]
	v_lshlrev_b32_e32 v112, 4, v226
	global_load_dwordx4 v[64:67], v112, s[8:9]
	global_load_dwordx4 v[68:71], v112, s[18:19]
	global_load_dwordx4 v[72:75], v112, s[16:17]
	global_load_dwordx4 v[76:79], v112, s[8:9] offset:1024
	global_load_dwordx4 v[80:83], v112, s[18:19] offset:1024
	global_load_dwordx4 v[84:87], v112, s[16:17] offset:1024
	global_load_dwordx4 v[88:91], v112, s[8:9] offset:2048
	global_load_dwordx4 v[92:95], v112, s[18:19] offset:2048
	global_load_dwordx4 v[96:99], v112, s[16:17] offset:2048
	global_load_dwordx4 v[100:103], v112, s[8:9] offset:3072
	global_load_dwordx4 v[104:107], v112, s[18:19] offset:3072
	global_load_dwordx4 v[108:111], v112, s[16:17] offset:3072
	v_lshl_add_u64 v[196:197], s[16:17], 0, v[196:197]
	v_pk_mul_f32 v[188:189], v[188:189], v[204:205] op_sel_hi:[1,0]
	v_pk_mul_f32 v[190:191], v[190:191], v[204:205] op_sel_hi:[1,0]
	v_lshrrev_b32_e32 v248, 1, v226
	v_pk_mul_f32 v[184:185], v[184:185], v[224:225] op_sel_hi:[1,0]
	v_pk_mul_f32 v[186:187], v[186:187], v[224:225] op_sel_hi:[1,0]
	v_pk_mul_f32 v[180:181], v[180:181], v[204:205] op_sel_hi:[1,0]
	v_pk_mul_f32 v[182:183], v[182:183], v[204:205] op_sel_hi:[1,0]
	v_pk_mul_f32 v[176:177], v[176:177], v[224:225] op_sel_hi:[1,0]
	v_pk_mul_f32 v[178:179], v[178:179], v[224:225] op_sel_hi:[1,0]
	v_pk_mul_f32 v[172:173], v[172:173], v[204:205] op_sel_hi:[1,0]
	v_pk_mul_f32 v[174:175], v[174:175], v[204:205] op_sel_hi:[1,0]
	v_pk_mul_f32 v[168:169], v[168:169], v[224:225] op_sel_hi:[1,0]
	v_pk_mul_f32 v[170:171], v[170:171], v[224:225] op_sel_hi:[1,0]
	v_pk_mul_f32 v[164:165], v[164:165], v[204:205] op_sel_hi:[1,0]
	v_pk_mul_f32 v[166:167], v[166:167], v[204:205] op_sel_hi:[1,0]
	v_pk_mul_f32 v[160:161], v[160:161], v[224:225] op_sel_hi:[1,0]
	v_pk_mul_f32 v[162:163], v[162:163], v[224:225] op_sel_hi:[1,0]
	v_pk_mul_f32 v[156:157], v[156:157], v[204:205] op_sel_hi:[1,0]
	v_pk_mul_f32 v[158:159], v[158:159], v[204:205] op_sel_hi:[1,0]
	v_pk_mul_f32 v[152:153], v[152:153], v[224:225] op_sel_hi:[1,0]
	v_pk_mul_f32 v[154:155], v[154:155], v[224:225] op_sel_hi:[1,0]
	v_pk_mul_f32 v[148:149], v[148:149], v[204:205] op_sel_hi:[1,0]
	v_pk_mul_f32 v[150:151], v[150:151], v[204:205] op_sel_hi:[1,0]
	v_pk_mul_f32 v[144:145], v[144:145], v[224:225] op_sel_hi:[1,0]
	v_pk_mul_f32 v[146:147], v[146:147], v[224:225] op_sel_hi:[1,0]
	v_pk_mul_f32 v[140:141], v[140:141], v[204:205] op_sel_hi:[1,0]
	v_pk_mul_f32 v[142:143], v[142:143], v[204:205] op_sel_hi:[1,0]
	v_pk_mul_f32 v[136:137], v[136:137], v[224:225] op_sel_hi:[1,0]
	v_pk_mul_f32 v[138:139], v[138:139], v[224:225] op_sel_hi:[1,0]
	v_pk_mul_f32 v[132:133], v[132:133], v[204:205] op_sel_hi:[1,0]
	v_pk_mul_f32 v[134:135], v[134:135], v[204:205] op_sel_hi:[1,0]
	v_pk_mul_f32 v[128:129], v[128:129], v[224:225] op_sel_hi:[1,0]
	v_pk_mul_f32 v[130:131], v[130:131], v[224:225] op_sel_hi:[1,0]
	s_waitcnt vmcnt(11)
	v_pk_mul_f32 v[244:245], v[188:189], v[64:65]
	v_pk_mul_f32 v[188:189], v[190:191], v[66:67]
	s_waitcnt vmcnt(10)
	v_pk_add_f32 v[68:69], v[68:69], 1.0 op_sel_hi:[1,0]
	v_pk_add_f32 v[70:71], v[70:71], 1.0 op_sel_hi:[1,0]
	s_waitcnt vmcnt(9)
	v_pk_fma_f32 v[190:191], v[244:245], v[68:69], v[72:73]
	v_pk_fma_f32 v[188:189], v[188:189], v[70:71], v[74:75]
	v_cvt_pk_bf16_f32 v244, v190, v191
	v_pk_mul_f32 v[64:65], v[184:185], v[64:65]
	v_lshlrev_b32_e32 v246, 16, v244
	v_and_b32_e32 v247, 0xffff0000, v244
	v_sub_f32_e32 v246, v190, v246
	v_sub_f32_e32 v247, v191, v247
	v_cvt_pk_bf16_f32 v245, v188, v189
	v_cvt_pk_bf16_f32 v246, v246, v247
	v_pk_mul_f32 v[184:185], v[186:187], v[66:67]
	v_lshlrev_b32_e32 v247, 16, v245
	v_and_b32_e32 v249, 0xffff0000, v245
	v_sub_f32_e32 v247, v188, v247
	v_sub_f32_e32 v249, v189, v249
	v_cvt_pk_bf16_f32 v247, v247, v249
	v_xor_b32_e32 v249, s27, v248
	v_lshlrev_b32_e32 v249, 4, v249
	v_add3_u32 v249, s28, v249, v207
	ds_write_b64 v249, v[244:245]
	v_add_u32_e32 v244, 0x10000, v249
	ds_write_b64 v244, v[246:247]
	v_pk_fma_f32 v[186:187], v[64:65], v[68:69], v[72:73]
	v_pk_fma_f32 v[184:185], v[184:185], v[70:71], v[74:75]
	v_cvt_pk_bf16_f32 v192, v186, v187
	v_lshlrev_b64 v[200:201], 2, v[220:221]
	v_lshlrev_b32_e32 v194, 16, v192
	v_and_b32_e32 v195, 0xffff0000, v192
	v_sub_f32_e32 v194, v186, v194
	v_sub_f32_e32 v195, v187, v195
	v_cvt_pk_bf16_f32 v193, v184, v185
	v_cvt_pk_bf16_f32 v194, v194, v195
	v_add_u32_e32 v249, 32, v248
	v_lshlrev_b32_e32 v195, 16, v193
	v_and_b32_e32 v196, 0xffff0000, v193
	v_sub_f32_e32 v195, v184, v195
	v_sub_f32_e32 v196, v185, v196
	v_cvt_pk_bf16_f32 v195, v195, v196
	v_xor_b32_e32 v196, s29, v248
	v_lshlrev_b32_e32 v196, 4, v196
	v_add3_u32 v196, s30, v196, v207
	ds_write_b64 v196, v[192:193]
	v_add_u32_e32 v192, 0x10000, v196
	ds_write_b64 v192, v[194:195]
	v_lshl_add_u64 v[192:193], s[8:9], 0, v[200:201]
	v_lshl_add_u64 v[196:197], s[18:19], 0, v[200:201]
	v_lshl_add_u64 v[200:201], s[16:17], 0, v[200:201]
	s_waitcnt vmcnt(8)
	v_pk_mul_f32 v[244:245], v[180:181], v[76:77]
	s_waitcnt vmcnt(7)
	v_pk_add_f32 v[80:81], v[80:81], 1.0 op_sel_hi:[1,0]
	v_pk_mul_f32 v[180:181], v[182:183], v[78:79]
	v_pk_add_f32 v[82:83], v[82:83], 1.0 op_sel_hi:[1,0]
	v_pk_mul_f32 v[76:77], v[176:177], v[76:77]
	v_pk_mul_f32 v[176:177], v[178:179], v[78:79]
	s_waitcnt vmcnt(6)
	v_pk_fma_f32 v[182:183], v[244:245], v[80:81], v[84:85]
	s_nop 0
	v_cvt_pk_bf16_f32 v244, v182, v183
	v_pk_fma_f32 v[180:181], v[180:181], v[82:83], v[86:87]
	v_lshlrev_b32_e32 v246, 16, v244
	v_and_b32_e32 v247, 0xffff0000, v244
	v_sub_f32_e32 v246, v182, v246
	v_sub_f32_e32 v247, v183, v247
	v_cvt_pk_bf16_f32 v245, v180, v181
	v_cvt_pk_bf16_f32 v246, v246, v247
	v_pk_fma_f32 v[178:179], v[76:77], v[80:81], v[84:85]
	v_lshlrev_b32_e32 v247, 16, v245
	v_and_b32_e32 v250, 0xffff0000, v245
	v_sub_f32_e32 v247, v180, v247
	v_sub_f32_e32 v250, v181, v250
	v_cvt_pk_bf16_f32 v247, v247, v250
	v_xor_b32_e32 v250, s27, v249
	v_lshlrev_b32_e32 v250, 4, v250
	v_add3_u32 v250, s28, v250, v207
	ds_write_b64 v250, v[244:245]
	v_add_u32_e32 v244, 0x10000, v250
	ds_write_b64 v244, v[246:247]
	v_cvt_pk_bf16_f32 v192, v178, v179
	v_pk_fma_f32 v[176:177], v[176:177], v[82:83], v[86:87]
	v_lshlrev_b32_e32 v194, 16, v192
	v_and_b32_e32 v195, 0xffff0000, v192
	v_sub_f32_e32 v194, v178, v194
	v_sub_f32_e32 v195, v179, v195
	v_cvt_pk_bf16_f32 v193, v176, v177
	v_cvt_pk_bf16_f32 v194, v194, v195
	v_lshlrev_b64 v[200:201], 2, v[218:219]
	v_lshlrev_b32_e32 v195, 16, v193
	v_and_b32_e32 v196, 0xffff0000, v193
	v_sub_f32_e32 v195, v176, v195
	v_sub_f32_e32 v196, v177, v196
	v_cvt_pk_bf16_f32 v195, v195, v196
	v_xor_b32_e32 v196, s29, v249
	v_lshlrev_b32_e32 v196, 4, v196
	v_add3_u32 v196, s30, v196, v207
	ds_write_b64 v196, v[192:193]
	v_add_u32_e32 v192, 0x10000, v196
	ds_write_b64 v192, v[194:195]
	v_lshl_add_u64 v[192:193], s[8:9], 0, v[200:201]
	v_lshl_add_u64 v[196:197], s[18:19], 0, v[200:201]
	v_lshl_add_u64 v[200:201], s[16:17], 0, v[200:201]
	v_add_u32_e32 v249, 64, v248
	s_waitcnt vmcnt(5)
	v_pk_mul_f32 v[244:245], v[172:173], v[88:89]
	v_pk_mul_f32 v[172:173], v[174:175], v[90:91]
	s_waitcnt vmcnt(4)
	v_pk_add_f32 v[92:93], v[92:93], 1.0 op_sel_hi:[1,0]
	v_pk_add_f32 v[94:95], v[94:95], 1.0 op_sel_hi:[1,0]
	s_waitcnt vmcnt(3)
	v_pk_fma_f32 v[174:175], v[244:245], v[92:93], v[96:97]
	v_pk_fma_f32 v[172:173], v[172:173], v[94:95], v[98:99]
	v_cvt_pk_bf16_f32 v244, v174, v175
	v_pk_mul_f32 v[88:89], v[168:169], v[88:89]
	v_lshlrev_b32_e32 v246, 16, v244
	v_and_b32_e32 v247, 0xffff0000, v244
	v_sub_f32_e32 v246, v174, v246
	v_sub_f32_e32 v247, v175, v247
	v_cvt_pk_bf16_f32 v245, v172, v173
	v_cvt_pk_bf16_f32 v246, v246, v247
	v_pk_mul_f32 v[168:169], v[170:171], v[90:91]
	v_lshlrev_b32_e32 v247, 16, v245
	v_and_b32_e32 v250, 0xffff0000, v245
	v_sub_f32_e32 v247, v172, v247
	v_sub_f32_e32 v250, v173, v250
	v_cvt_pk_bf16_f32 v247, v247, v250
	v_xor_b32_e32 v250, s27, v249
	v_lshlrev_b32_e32 v250, 4, v250
	v_add3_u32 v250, s28, v250, v207
	ds_write_b64 v250, v[244:245]
	v_add_u32_e32 v244, 0x10000, v250
	ds_write_b64 v244, v[246:247]
	v_pk_fma_f32 v[170:171], v[88:89], v[92:93], v[96:97]
	v_pk_fma_f32 v[168:169], v[168:169], v[94:95], v[98:99]
	v_cvt_pk_bf16_f32 v192, v170, v171
	v_lshlrev_b64 v[200:201], 2, v[216:217]
	v_lshlrev_b32_e32 v194, 16, v192
	v_and_b32_e32 v195, 0xffff0000, v192
	v_sub_f32_e32 v194, v170, v194
	v_sub_f32_e32 v195, v171, v195
	v_cvt_pk_bf16_f32 v193, v168, v169
	v_cvt_pk_bf16_f32 v194, v194, v195
	s_nop 0
	v_lshlrev_b32_e32 v195, 16, v193
	v_and_b32_e32 v196, 0xffff0000, v193
	v_sub_f32_e32 v195, v168, v195
	v_sub_f32_e32 v196, v169, v196
	v_cvt_pk_bf16_f32 v195, v195, v196
	v_xor_b32_e32 v196, s29, v249
	v_lshlrev_b32_e32 v196, 4, v196
	v_add3_u32 v196, s30, v196, v207
	ds_write_b64 v196, v[192:193]
	v_add_u32_e32 v192, 0x10000, v196
	ds_write_b64 v192, v[194:195]
	v_lshl_add_u64 v[192:193], s[8:9], 0, v[200:201]
	v_lshl_add_u64 v[196:197], s[18:19], 0, v[200:201]
	v_lshl_add_u64 v[200:201], s[16:17], 0, v[200:201]
	v_add_u32_e32 v249, 0x60, v248
	s_waitcnt vmcnt(2)
	v_pk_mul_f32 v[244:245], v[164:165], v[100:101]
	v_pk_mul_f32 v[164:165], v[166:167], v[102:103]
	s_waitcnt vmcnt(1)
	v_pk_add_f32 v[104:105], v[104:105], 1.0 op_sel_hi:[1,0]
	v_pk_add_f32 v[106:107], v[106:107], 1.0 op_sel_hi:[1,0]
	s_waitcnt vmcnt(0)
	v_pk_fma_f32 v[166:167], v[244:245], v[104:105], v[108:109]
	v_pk_fma_f32 v[164:165], v[164:165], v[106:107], v[110:111]
	v_cvt_pk_bf16_f32 v244, v166, v167
	v_pk_mul_f32 v[100:101], v[160:161], v[100:101]
	v_lshlrev_b32_e32 v246, 16, v244
	v_and_b32_e32 v247, 0xffff0000, v244
	v_sub_f32_e32 v246, v166, v246
	v_sub_f32_e32 v247, v167, v247
	v_cvt_pk_bf16_f32 v245, v164, v165
	v_cvt_pk_bf16_f32 v246, v246, v247
	v_pk_mul_f32 v[160:161], v[162:163], v[102:103]
	v_lshlrev_b32_e32 v247, 16, v245
	v_and_b32_e32 v250, 0xffff0000, v245
	v_sub_f32_e32 v247, v164, v247
	v_sub_f32_e32 v250, v165, v250
	v_cvt_pk_bf16_f32 v247, v247, v250
	v_xor_b32_e32 v250, s27, v249
	v_lshlrev_b32_e32 v250, 4, v250
	v_add3_u32 v250, s28, v250, v207
	ds_write_b64 v250, v[244:245]
	v_add_u32_e32 v244, 0x10000, v250
	ds_write_b64 v244, v[246:247]
	v_pk_fma_f32 v[162:163], v[100:101], v[104:105], v[108:109]
	v_pk_fma_f32 v[160:161], v[160:161], v[106:107], v[110:111]
	v_cvt_pk_bf16_f32 v192, v162, v163
	v_lshlrev_b64 v[200:201], 2, v[214:215]
	v_lshlrev_b32_e32 v194, 16, v192
	v_and_b32_e32 v195, 0xffff0000, v192
	v_sub_f32_e32 v194, v162, v194
	v_sub_f32_e32 v195, v163, v195
	v_cvt_pk_bf16_f32 v193, v160, v161
	v_cvt_pk_bf16_f32 v194, v194, v195
	s_nop 0
	v_lshlrev_b32_e32 v195, 16, v193
	v_and_b32_e32 v196, 0xffff0000, v193
	v_sub_f32_e32 v195, v160, v195
	v_sub_f32_e32 v196, v161, v196
	v_cvt_pk_bf16_f32 v195, v195, v196
	v_xor_b32_e32 v196, s29, v249
	v_lshlrev_b32_e32 v196, 4, v196
	v_add3_u32 v196, s30, v196, v207
	ds_write_b64 v196, v[192:193]
	v_add_u32_e32 v192, 0x10000, v196
	ds_write_b64 v192, v[194:195]
	v_lshl_add_u64 v[192:193], s[8:9], 0, v[200:201]
	v_lshl_add_u64 v[196:197], s[18:19], 0, v[200:201]
	v_add_u32_e32 v112, 0x1000, v112
	global_load_dwordx4 v[64:67], v112, s[8:9]
	global_load_dwordx4 v[68:71], v112, s[18:19]
	global_load_dwordx4 v[72:75], v112, s[16:17]
	global_load_dwordx4 v[76:79], v112, s[8:9] offset:1024
	global_load_dwordx4 v[80:83], v112, s[18:19] offset:1024
	global_load_dwordx4 v[84:87], v112, s[16:17] offset:1024
	global_load_dwordx4 v[88:91], v112, s[8:9] offset:2048
	global_load_dwordx4 v[92:95], v112, s[18:19] offset:2048
	global_load_dwordx4 v[96:99], v112, s[16:17] offset:2048
	global_load_dwordx4 v[100:103], v112, s[8:9] offset:3072
	global_load_dwordx4 v[104:107], v112, s[18:19] offset:3072
	global_load_dwordx4 v[108:111], v112, s[16:17] offset:3072
	v_lshl_add_u64 v[200:201], s[16:17], 0, v[200:201]
	v_add_u32_e32 v249, 0x80, v248
	s_waitcnt vmcnt(11)
	v_pk_mul_f32 v[244:245], v[156:157], v[64:65]
	v_pk_mul_f32 v[156:157], v[158:159], v[66:67]
	s_waitcnt vmcnt(10)
	v_pk_add_f32 v[68:69], v[68:69], 1.0 op_sel_hi:[1,0]
	v_pk_add_f32 v[70:71], v[70:71], 1.0 op_sel_hi:[1,0]
	s_waitcnt vmcnt(9)
	v_pk_fma_f32 v[158:159], v[244:245], v[68:69], v[72:73]
	v_pk_fma_f32 v[156:157], v[156:157], v[70:71], v[74:75]
	v_cvt_pk_bf16_f32 v244, v158, v159
	v_pk_mul_f32 v[64:65], v[152:153], v[64:65]
	v_lshlrev_b32_e32 v246, 16, v244
	v_and_b32_e32 v247, 0xffff0000, v244
	v_sub_f32_e32 v246, v158, v246
	v_sub_f32_e32 v247, v159, v247
	v_cvt_pk_bf16_f32 v245, v156, v157
	v_cvt_pk_bf16_f32 v246, v246, v247
	v_pk_mul_f32 v[152:153], v[154:155], v[66:67]
	v_lshlrev_b32_e32 v247, 16, v245
	v_and_b32_e32 v250, 0xffff0000, v245
	v_sub_f32_e32 v247, v156, v247
	v_sub_f32_e32 v250, v157, v250
	v_cvt_pk_bf16_f32 v247, v247, v250
	v_xor_b32_e32 v250, s27, v249
	v_lshlrev_b32_e32 v250, 4, v250
	v_add3_u32 v250, s28, v250, v207
	ds_write_b64 v250, v[244:245]
	v_add_u32_e32 v244, 0x10000, v250
	ds_write_b64 v244, v[246:247]
	v_pk_fma_f32 v[154:155], v[64:65], v[68:69], v[72:73]
	v_pk_fma_f32 v[152:153], v[152:153], v[70:71], v[74:75]
	v_cvt_pk_bf16_f32 v192, v154, v155
	v_lshlrev_b64 v[200:201], 2, v[212:213]
	v_lshlrev_b32_e32 v194, 16, v192
	v_and_b32_e32 v195, 0xffff0000, v192
	v_sub_f32_e32 v194, v154, v194
	v_sub_f32_e32 v195, v155, v195
	v_cvt_pk_bf16_f32 v193, v152, v153
	v_cvt_pk_bf16_f32 v194, v194, v195
	s_nop 0
	v_lshlrev_b32_e32 v195, 16, v193
	v_and_b32_e32 v196, 0xffff0000, v193
	v_sub_f32_e32 v195, v152, v195
	v_sub_f32_e32 v196, v153, v196
	v_cvt_pk_bf16_f32 v195, v195, v196
	v_xor_b32_e32 v196, s29, v249
	v_lshlrev_b32_e32 v196, 4, v196
	v_add3_u32 v196, s30, v196, v207
	ds_write_b64 v196, v[192:193]
	v_add_u32_e32 v192, 0x10000, v196
	ds_write_b64 v192, v[194:195]
	v_lshl_add_u64 v[192:193], s[8:9], 0, v[200:201]
	v_lshl_add_u64 v[196:197], s[18:19], 0, v[200:201]
	v_lshl_add_u64 v[200:201], s[16:17], 0, v[200:201]
	v_add_u32_e32 v249, 0xa0, v248
	s_waitcnt vmcnt(8)
	v_pk_mul_f32 v[244:245], v[148:149], v[76:77]
	v_pk_mul_f32 v[148:149], v[150:151], v[78:79]
	s_waitcnt vmcnt(7)
	v_pk_add_f32 v[80:81], v[80:81], 1.0 op_sel_hi:[1,0]
	v_pk_add_f32 v[82:83], v[82:83], 1.0 op_sel_hi:[1,0]
	s_waitcnt vmcnt(6)
	v_pk_fma_f32 v[150:151], v[244:245], v[80:81], v[84:85]
	v_pk_fma_f32 v[148:149], v[148:149], v[82:83], v[86:87]
	v_cvt_pk_bf16_f32 v244, v150, v151
	v_pk_mul_f32 v[76:77], v[144:145], v[76:77]
	v_lshlrev_b32_e32 v246, 16, v244
	v_and_b32_e32 v247, 0xffff0000, v244
	v_sub_f32_e32 v246, v150, v246
	v_sub_f32_e32 v247, v151, v247
	v_cvt_pk_bf16_f32 v245, v148, v149
	v_cvt_pk_bf16_f32 v246, v246, v247
	v_pk_mul_f32 v[144:145], v[146:147], v[78:79]
	v_lshlrev_b32_e32 v247, 16, v245
	v_and_b32_e32 v250, 0xffff0000, v245
	v_sub_f32_e32 v247, v148, v247
	v_sub_f32_e32 v250, v149, v250
	v_cvt_pk_bf16_f32 v247, v247, v250
	v_xor_b32_e32 v250, s27, v249
	v_lshlrev_b32_e32 v250, 4, v250
	v_add3_u32 v250, s28, v250, v207
	ds_write_b64 v250, v[244:245]
	v_add_u32_e32 v244, 0x10000, v250
	ds_write_b64 v244, v[246:247]
	v_pk_fma_f32 v[146:147], v[76:77], v[80:81], v[84:85]
	v_pk_fma_f32 v[144:145], v[144:145], v[82:83], v[86:87]
	v_cvt_pk_bf16_f32 v192, v146, v147
	v_lshlrev_b64 v[200:201], 2, v[210:211]
	v_lshlrev_b32_e32 v194, 16, v192
	v_and_b32_e32 v195, 0xffff0000, v192
	v_sub_f32_e32 v194, v146, v194
	v_sub_f32_e32 v195, v147, v195
	v_cvt_pk_bf16_f32 v193, v144, v145
	v_cvt_pk_bf16_f32 v194, v194, v195
	s_nop 0
	v_lshlrev_b32_e32 v195, 16, v193
	v_and_b32_e32 v196, 0xffff0000, v193
	v_sub_f32_e32 v195, v144, v195
	v_sub_f32_e32 v196, v145, v196
	v_cvt_pk_bf16_f32 v195, v195, v196
	v_xor_b32_e32 v196, s29, v249
	v_lshlrev_b32_e32 v196, 4, v196
	v_add3_u32 v196, s30, v196, v207
	ds_write_b64 v196, v[192:193]
	v_add_u32_e32 v192, 0x10000, v196
	ds_write_b64 v192, v[194:195]
	v_lshl_add_u64 v[192:193], s[8:9], 0, v[200:201]
	v_lshl_add_u64 v[196:197], s[18:19], 0, v[200:201]
	v_lshl_add_u64 v[200:201], s[16:17], 0, v[200:201]
	v_add_u32_e32 v249, 0xc0, v248
	v_add_u32_e32 v248, 0xe0, v248
	s_waitcnt vmcnt(5)
	v_pk_mul_f32 v[244:245], v[140:141], v[88:89]
	v_pk_mul_f32 v[140:141], v[142:143], v[90:91]
	s_waitcnt vmcnt(4)
	v_pk_add_f32 v[92:93], v[92:93], 1.0 op_sel_hi:[1,0]
	v_pk_add_f32 v[94:95], v[94:95], 1.0 op_sel_hi:[1,0]
	s_waitcnt vmcnt(3)
	v_pk_fma_f32 v[142:143], v[244:245], v[92:93], v[96:97]
	v_pk_fma_f32 v[140:141], v[140:141], v[94:95], v[98:99]
	v_cvt_pk_bf16_f32 v244, v142, v143
	v_pk_mul_f32 v[88:89], v[136:137], v[88:89]
	v_lshlrev_b32_e32 v246, 16, v244
	v_and_b32_e32 v247, 0xffff0000, v244
	v_sub_f32_e32 v246, v142, v246
	v_sub_f32_e32 v247, v143, v247
	v_cvt_pk_bf16_f32 v245, v140, v141
	v_cvt_pk_bf16_f32 v246, v246, v247
	v_pk_mul_f32 v[136:137], v[138:139], v[90:91]
	v_lshlrev_b32_e32 v247, 16, v245
	v_and_b32_e32 v250, 0xffff0000, v245
	v_sub_f32_e32 v247, v140, v247
	v_sub_f32_e32 v250, v141, v250
	v_cvt_pk_bf16_f32 v247, v247, v250
	v_xor_b32_e32 v250, s27, v249
	v_lshlrev_b32_e32 v250, 4, v250
	v_add3_u32 v250, s28, v250, v207
	ds_write_b64 v250, v[244:245]
	v_add_u32_e32 v244, 0x10000, v250
	ds_write_b64 v244, v[246:247]
	v_pk_fma_f32 v[138:139], v[88:89], v[92:93], v[96:97]
	v_pk_fma_f32 v[136:137], v[136:137], v[94:95], v[98:99]
	v_cvt_pk_bf16_f32 v192, v138, v139
	v_lshlrev_b64 v[200:201], 2, v[208:209]
	v_lshlrev_b32_e32 v194, 16, v192
	v_and_b32_e32 v195, 0xffff0000, v192
	v_sub_f32_e32 v194, v138, v194
	v_sub_f32_e32 v195, v139, v195
	v_cvt_pk_bf16_f32 v193, v136, v137
	v_cvt_pk_bf16_f32 v194, v194, v195
	s_nop 0
	v_lshlrev_b32_e32 v195, 16, v193
	v_and_b32_e32 v196, 0xffff0000, v193
	v_sub_f32_e32 v195, v136, v195
	v_sub_f32_e32 v196, v137, v196
	v_cvt_pk_bf16_f32 v195, v195, v196
	v_xor_b32_e32 v196, s29, v249
	v_lshlrev_b32_e32 v196, 4, v196
	v_add3_u32 v196, s30, v196, v207
	ds_write_b64 v196, v[192:193]
	v_add_u32_e32 v192, 0x10000, v196
	ds_write_b64 v192, v[194:195]
	v_lshl_add_u64 v[192:193], s[8:9], 0, v[200:201]
	v_lshl_add_u64 v[196:197], s[18:19], 0, v[200:201]
	v_lshl_add_u64 v[200:201], s[16:17], 0, v[200:201]
	s_lshl_b64 s[16:17], s[12:13], 11
	s_add_u32 s16, s23, s16
	s_addc_u32 s17, s24, s17
	s_lshl_b64 s[4:5], s[4:5], 11
	s_add_u32 s4, s23, s4
	s_addc_u32 s5, s24, s5
	s_waitcnt vmcnt(2)
	v_pk_mul_f32 v[244:245], v[132:133], v[100:101]
	v_pk_mul_f32 v[132:133], v[134:135], v[102:103]
	s_waitcnt vmcnt(1)
	v_pk_add_f32 v[104:105], v[104:105], 1.0 op_sel_hi:[1,0]
	v_pk_add_f32 v[106:107], v[106:107], 1.0 op_sel_hi:[1,0]
	s_waitcnt vmcnt(0)
	v_pk_fma_f32 v[134:135], v[244:245], v[104:105], v[108:109]
	v_pk_fma_f32 v[132:133], v[132:133], v[106:107], v[110:111]
	v_cvt_pk_bf16_f32 v244, v134, v135
	v_pk_mul_f32 v[100:101], v[128:129], v[100:101]
	v_lshlrev_b32_e32 v204, 16, v244
	v_and_b32_e32 v246, 0xffff0000, v244
	v_sub_f32_e32 v204, v134, v204
	v_sub_f32_e32 v246, v135, v246
	v_cvt_pk_bf16_f32 v245, v132, v133
	v_cvt_pk_bf16_f32 v246, v204, v246
	v_pk_mul_f32 v[128:129], v[130:131], v[102:103]
	v_lshlrev_b32_e32 v204, 16, v245
	v_and_b32_e32 v247, 0xffff0000, v245
	v_sub_f32_e32 v204, v132, v204
	v_sub_f32_e32 v247, v133, v247
	v_cvt_pk_bf16_f32 v247, v204, v247
	v_xor_b32_e32 v204, s27, v248
	v_lshlrev_b32_e32 v204, 4, v204
	v_add3_u32 v204, s28, v204, v207
	ds_write_b64 v204, v[244:245]
	v_add_u32_e32 v204, 0x10000, v204
	ds_write_b64 v204, v[246:247]
	v_pk_fma_f32 v[130:131], v[100:101], v[104:105], v[108:109]
	v_pk_fma_f32 v[128:129], v[128:129], v[106:107], v[110:111]
	s_cmp_lt_i32 s41, s44
	s_cbranch_scc0 .Lpf_skip_g
	s_add_i32 s98, s33, s12
	s_ashr_i32 s99, s98, 31
	s_lshl_b64 s[98:99], s[98:99], 13
	s_add_u32 s98, s6, s98
	s_addc_u32 s99, s7, s99
	v_lshlrev_b64 v[96:97], 2, v[222:223]
	v_lshlrev_b64 v[112:113], 2, v[214:215]
	v_lshlrev_b64 v[114:115], 2, v[212:213]
	v_lshlrev_b64 v[120:121], 2, v[210:211]
	v_lshlrev_b64 v[122:123], 2, v[208:209]
	v_lshl_add_u64 v[76:77], s[98:99], 0, v[96:97]
	v_lshl_add_u64 v[80:81], s[98:99], 0, v[112:113]
	v_lshl_add_u64 v[84:85], s[98:99], 0, v[114:115]
	v_lshl_add_u64 v[88:89], s[98:99], 0, v[120:121]
	v_lshl_add_u64 v[92:93], s[98:99], 0, v[122:123]
	s_add_i32 s98, s31, s12
	s_ashr_i32 s99, s98, 31
	s_lshl_b64 s[98:99], s[98:99], 13
	s_add_u32 s98, s6, s98
	s_addc_u32 s99, s7, s99
	v_lshl_add_u64 v[108:109], s[98:99], 0, v[96:97]
	global_load_dwordx4 v[64:67], v[76:77], off
	global_load_dwordx4 v[68:71], v[76:77], off offset:1024
	global_load_dwordx4 v[72:75], v[76:77], off offset:2048
	s_nop 0
	global_load_dwordx4 v[76:79], v[76:77], off offset:3072
	s_nop 0
	global_load_dwordx4 v[80:83], v[80:81], off
	s_nop 0
	global_load_dwordx4 v[84:87], v[84:85], off
	s_nop 0
	global_load_dwordx4 v[88:91], v[88:89], off
	s_nop 0
	global_load_dwordx4 v[92:95], v[92:93], off
	s_nop 0
	global_load_dwordx4 v[96:99], v[108:109], off
	global_load_dwordx4 v[100:103], v[108:109], off offset:1024
	global_load_dwordx4 v[104:107], v[108:109], off offset:2048
	s_nop 0
	global_load_dwordx4 v[108:111], v[108:109], off offset:3072
	v_lshl_add_u64 v[112:113], s[98:99], 0, v[112:113]
	v_lshl_add_u64 v[116:117], s[98:99], 0, v[114:115]
	v_lshl_add_u64 v[120:121], s[98:99], 0, v[120:121]
	v_lshl_add_u64 v[124:125], s[98:99], 0, v[122:123]
	global_load_dwordx4 v[112:115], v[112:113], off
	s_nop 0
	global_load_dwordx4 v[116:119], v[116:117], off
	s_nop 0
	global_load_dwordx4 v[120:123], v[120:121], off
	s_nop 0
	global_load_dwordx4 v[124:127], v[124:125], off
.Lpf_skip_g:
	v_cvt_pk_bf16_f32 v192, v130, v131
	s_nop 0
	v_lshlrev_b32_e32 v194, 16, v192
	v_and_b32_e32 v195, 0xffff0000, v192
	v_sub_f32_e32 v194, v130, v194
	v_sub_f32_e32 v195, v131, v195
	v_cvt_pk_bf16_f32 v193, v128, v129
	v_cvt_pk_bf16_f32 v194, v194, v195
	s_nop 0
	v_lshlrev_b32_e32 v195, 16, v193
	v_and_b32_e32 v196, 0xffff0000, v193
	v_sub_f32_e32 v195, v128, v195
	v_sub_f32_e32 v196, v129, v196
	v_cvt_pk_bf16_f32 v195, v195, v196
	v_xor_b32_e32 v196, s29, v248
	v_lshlrev_b32_e32 v196, 4, v196
	v_add3_u32 v196, s30, v196, v207
	ds_write_b64 v196, v[192:193]
	v_add_u32_e32 v192, 0x10000, v196
	ds_write_b64 v192, v[194:195]
	v_mov_b32_e32 v192, 0
	v_cvt_pk_fp8_f32 v192, v190, v191
	v_cvt_pk_fp8_f32 v192, v188, v189 op_sel:[0,0,1]
	v_lshl_add_u64 v[188:189], s[16:17], 0, v[222:223]
	global_store_dword v[188:189], v192, off
	v_mov_b32_e32 v188, 0
	v_cvt_pk_fp8_f32 v188, v182, v183
	v_cvt_pk_fp8_f32 v188, v180, v181 op_sel:[0,0,1]
	v_lshl_add_u64 v[180:181], s[16:17], 0, v[220:221]
	global_store_dword v[180:181], v188, off
	v_mov_b32_e32 v180, 0
	v_cvt_pk_fp8_f32 v180, v174, v175
	v_cvt_pk_fp8_f32 v180, v172, v173 op_sel:[0,0,1]
	v_lshl_add_u64 v[172:173], s[16:17], 0, v[218:219]
	global_store_dword v[172:173], v180, off
	v_mov_b32_e32 v172, 0
	v_cvt_pk_fp8_f32 v172, v166, v167
	v_cvt_pk_fp8_f32 v172, v164, v165 op_sel:[0,0,1]
	v_lshl_add_u64 v[164:165], s[16:17], 0, v[216:217]
	global_store_dword v[164:165], v172, off
	v_mov_b32_e32 v164, 0
	v_cvt_pk_fp8_f32 v164, v158, v159
	v_cvt_pk_fp8_f32 v164, v156, v157 op_sel:[0,0,1]
	v_lshl_add_u64 v[156:157], s[16:17], 0, v[214:215]
	global_store_dword v[156:157], v164, off
	v_mov_b32_e32 v156, 0
	v_cvt_pk_fp8_f32 v156, v150, v151
	v_cvt_pk_fp8_f32 v156, v148, v149 op_sel:[0,0,1]
	v_lshl_add_u64 v[148:149], s[16:17], 0, v[212:213]
	global_store_dword v[148:149], v156, off
	v_mov_b32_e32 v148, 0
	v_cvt_pk_fp8_f32 v148, v142, v143
	v_cvt_pk_fp8_f32 v148, v140, v141 op_sel:[0,0,1]
	v_lshl_add_u64 v[140:141], s[16:17], 0, v[210:211]
	global_store_dword v[140:141], v148, off
	v_mov_b32_e32 v140, 0
	v_cvt_pk_fp8_f32 v140, v134, v135
	v_mov_b32_e32 v134, 0
	v_cvt_pk_fp8_f32 v134, v186, v187
	v_cvt_pk_fp8_f32 v140, v132, v133 op_sel:[0,0,1]
	v_lshl_add_u64 v[132:133], s[16:17], 0, v[208:209]
	v_cvt_pk_fp8_f32 v134, v184, v185 op_sel:[0,0,1]
	global_store_dword v[132:133], v140, off
	v_lshl_add_u64 v[132:133], s[4:5], 0, v[222:223]
	global_store_dword v[132:133], v134, off
	v_mov_b32_e32 v134, 0
	v_cvt_pk_fp8_f32 v134, v178, v179
	v_lshl_add_u64 v[132:133], s[4:5], 0, v[220:221]
	v_cvt_pk_fp8_f32 v134, v176, v177 op_sel:[0,0,1]
	global_store_dword v[132:133], v134, off
	v_mov_b32_e32 v134, 0
	v_cvt_pk_fp8_f32 v134, v170, v171
	v_lshl_add_u64 v[132:133], s[4:5], 0, v[218:219]
	v_cvt_pk_fp8_f32 v134, v168, v169 op_sel:[0,0,1]
	global_store_dword v[132:133], v134, off
	v_mov_b32_e32 v134, 0
	v_cvt_pk_fp8_f32 v134, v162, v163
	v_lshl_add_u64 v[132:133], s[4:5], 0, v[216:217]
	v_cvt_pk_fp8_f32 v134, v160, v161 op_sel:[0,0,1]
	global_store_dword v[132:133], v134, off
	v_mov_b32_e32 v134, 0
	v_cvt_pk_fp8_f32 v134, v154, v155
	v_lshl_add_u64 v[132:133], s[4:5], 0, v[214:215]
	v_cvt_pk_fp8_f32 v134, v152, v153 op_sel:[0,0,1]
	global_store_dword v[132:133], v134, off
	v_mov_b32_e32 v134, 0
	v_cvt_pk_fp8_f32 v134, v146, v147
	v_lshl_add_u64 v[132:133], s[4:5], 0, v[212:213]
	v_cvt_pk_fp8_f32 v134, v144, v145 op_sel:[0,0,1]
	global_store_dword v[132:133], v134, off
	v_mov_b32_e32 v134, 0
	v_cvt_pk_fp8_f32 v134, v138, v139
	v_lshl_add_u64 v[132:133], s[4:5], 0, v[210:211]
	v_cvt_pk_fp8_f32 v134, v136, v137 op_sel:[0,0,1]
	global_store_dword v[132:133], v134, off
	v_mov_b32_e32 v132, 0
	v_cvt_pk_fp8_f32 v132, v130, v131
	v_cvt_pk_fp8_f32 v132, v128, v129 op_sel:[0,0,1]
	v_lshl_add_u64 v[128:129], s[4:5], 0, v[208:209]
	global_store_dword v[128:129], v132, off
	s_waitcnt lgkmcnt(0)
	s_barrier
	ds_read_b128 v[128:131], v227
	s_waitcnt lgkmcnt(0)
	v_mfma_f32_16x16x32_bf16 v[136:139], v[0:3], v[128:131], 0
	v_add_u32_e32 v132, 0x10000, v227
	ds_read_b128 v[132:135], v132
	v_mfma_f32_16x16x32_bf16 v[128:131], v[4:7], v[128:131], v[136:139]
	s_nop 4
	v_add_u32_e32 v136, 0x10000, v228
	ds_read_b128 v[136:139], v136
	s_waitcnt lgkmcnt(1)
	v_mfma_f32_16x16x32_bf16 v[128:131], v[0:3], v[132:135], v[128:131]
	ds_read_b128 v[132:135], v228
	s_waitcnt lgkmcnt(0)
	v_mfma_f32_16x16x32_bf16 v[128:131], v[8:11], v[132:135], v[128:131]
	v_mfma_f32_16x16x32_bf16 v[128:131], v[12:15], v[132:135], v[128:131]
	v_mfma_f32_16x16x32_bf16 v[128:131], v[8:11], v[136:139], v[128:131]
	ds_read_b128 v[132:135], v229
	ds_read_b128 v[136:139], v230
	s_waitcnt lgkmcnt(1)
	v_mfma_f32_16x16x32_bf16 v[128:131], v[16:19], v[132:135], v[128:131]
	v_mfma_f32_16x16x32_bf16 v[128:131], v[20:23], v[132:135], v[128:131]
	s_waitcnt lgkmcnt(0)
	v_mfma_f32_16x16x32_bf16 v[128:131], v[16:19], v[136:139], v[128:131]
	ds_read_b128 v[132:135], v231
	ds_read_b128 v[136:139], v232
	s_waitcnt lgkmcnt(1)
	v_mfma_f32_16x16x32_bf16 v[128:131], v[24:27], v[132:135], v[128:131]
	v_mfma_f32_16x16x32_bf16 v[128:131], v[28:31], v[132:135], v[128:131]
	s_waitcnt lgkmcnt(0)
	v_mfma_f32_16x16x32_bf16 v[128:131], v[24:27], v[136:139], v[128:131]
	ds_read_b128 v[132:135], v233
	ds_read_b128 v[136:139], v234
	s_waitcnt lgkmcnt(1)
	v_mfma_f32_16x16x32_bf16 v[128:131], v[32:35], v[132:135], v[128:131]
	v_mfma_f32_16x16x32_bf16 v[128:131], v[36:39], v[132:135], v[128:131]
	s_waitcnt lgkmcnt(0)
	v_mfma_f32_16x16x32_bf16 v[128:131], v[32:35], v[136:139], v[128:131]
	ds_read_b128 v[132:135], v235
	ds_read_b128 v[136:139], v236
	s_waitcnt lgkmcnt(1)
	v_mfma_f32_16x16x32_bf16 v[128:131], v[40:43], v[132:135], v[128:131]
	v_mfma_f32_16x16x32_bf16 v[128:131], v[44:47], v[132:135], v[128:131]
	s_waitcnt lgkmcnt(0)
	v_mfma_f32_16x16x32_bf16 v[128:131], v[40:43], v[136:139], v[128:131]
	ds_read_b128 v[132:135], v237
	ds_read_b128 v[136:139], v238
	s_waitcnt lgkmcnt(1)
	v_mfma_f32_16x16x32_bf16 v[128:131], v[48:51], v[132:135], v[128:131]
	v_mfma_f32_16x16x32_bf16 v[128:131], v[52:55], v[132:135], v[128:131]
	s_waitcnt lgkmcnt(0)
	v_mfma_f32_16x16x32_bf16 v[128:131], v[48:51], v[136:139], v[128:131]
	ds_read_b128 v[132:135], v239
	ds_read_b128 v[136:139], v240
	s_waitcnt lgkmcnt(1)
	v_mfma_f32_16x16x32_bf16 v[128:131], v[56:59], v[132:135], v[128:131]
	v_mfma_f32_16x16x32_bf16 v[128:131], v[60:63], v[132:135], v[128:131]
	s_waitcnt lgkmcnt(0)
	v_mfma_f32_16x16x32_bf16 v[128:131], v[56:59], v[136:139], v[128:131]
	s_nop 7
	ds_write_b128 v243, v[128:131]
	v_mov_b32_e32 v128, v225
	s_waitcnt lgkmcnt(0)
	s_barrier
	s_nop 0
	v_cmp_gt_i32_e32 vcc, s35, v128
	s_and_saveexec_b64 s[4:5], vcc
	s_cbranch_execz .LBB0_152
	v_lshlrev_b32_e32 v129, 2, v128
	v_and_b32_e32 v204, 28, v129
	global_load_dword v138, v204, s[10:11]
	v_ashrrev_i32_e32 v129, 3, v128
	s_add_i32 s13, 0, 0x22000
	v_ashrrev_i32_e32 v136, 4, v128
	v_lshlrev_b32_e32 v128, 6, v129
	v_and_b32_e32 v129, 1, v129
	v_add3_u32 v134, s13, v128, v204
	v_add_u32_e32 v137, s0, v129
	ds_read2st64_b32 v[128:129], v134 offset1:4
	ds_read2st64_b32 v[130:131], v134 offset0:8 offset1:12
	ds_read2st64_b32 v[132:133], v134 offset0:16 offset1:20
	ds_read2st64_b32 v[134:135], v134 offset0:24 offset1:28
	v_mul_lo_u32 v137, v137, s21
	s_waitcnt lgkmcnt(3)
	v_add_f32_e32 v128, 0, v128
	v_add_f32_e32 v128, v128, v129
	s_waitcnt lgkmcnt(2)
	v_add_f32_e32 v128, v128, v130
	v_add_f32_e32 v128, v128, v131
	s_waitcnt lgkmcnt(1)
	v_add_f32_e32 v128, v128, v132
	v_add_f32_e32 v128, v128, v133
	s_waitcnt lgkmcnt(0)
	v_add_f32_e32 v128, v128, v134
	v_add_f32_e32 v128, v128, v135
	v_add3_u32 v136, v136, s22, v137
	v_ashrrev_i32_e32 v137, 31, v136
	s_waitcnt vmcnt(0)
	v_add_f32_e32 v130, v128, v138
	v_mul_f32_e64 v128, |v130|, s36
	v_exp_f32_e32 v144, v128
	v_min_f32_e32 v145, 0, v130
	v_lshlrev_b64 v[128:129], 5, v[136:137]
	v_lshl_add_u64 v[128:129], s[14:15], 0, v[128:129]
	v_add_f32_e32 v132, 1.0, v144
	v_add_f32_e32 v133, -1.0, v132
	v_frexp_mant_f32_e32 v134, v132
	v_cvt_f64_f32_e32 v[130:131], v132
	v_sub_f32_e32 v135, v133, v132
	v_frexp_exp_i32_f64_e32 v130, v[130:131]
	v_cmp_gt_f32_e32 vcc, s37, v134
	v_sub_f32_e32 v133, v144, v133
	v_add_f32_e32 v131, 1.0, v135
	v_subbrev_co_u32_e32 v130, vcc, 0, v130, vcc
	v_add_f32_e32 v131, v133, v131
	v_sub_u32_e32 v133, 0, v130
	v_ldexp_f32 v132, v132, v133
	v_add_f32_e32 v134, -1.0, v132
	v_add_f32_e32 v135, 1.0, v132
	v_ldexp_f32 v131, v131, v133
	v_add_f32_e32 v133, 1.0, v134
	v_add_f32_e32 v136, -1.0, v135
	v_sub_f32_e32 v133, v132, v133
	v_sub_f32_e32 v132, v132, v136
	v_add_f32_e32 v136, v131, v133
	v_add_f32_e32 v131, v131, v132
	v_add_f32_e32 v138, v135, v131
	v_rcp_f32_e32 v139, v138
	v_add_f32_e32 v133, v134, v136
	v_sub_f32_e32 v134, v133, v134
	v_sub_f32_e32 v132, v138, v135
	v_mul_f32_e32 v141, v133, v139
	v_sub_f32_e32 v140, v136, v134
	v_mul_f32_e32 v134, v138, v141
	v_sub_f32_e32 v131, v131, v132
	v_fma_f32 v136, v141, v138, -v134
	v_fmac_f32_e32 v136, v141, v131
	v_add_f32_e32 v132, v134, v136
	v_sub_f32_e32 v135, v133, v132
	v_mov_b32_e32 v137, v132
	v_pk_add_f32 v[132:133], v[132:133], v[134:135] neg_lo:[0,1] neg_hi:[0,1]
	v_cvt_f32_i32_e32 v130, v130
	v_pk_add_f32 v[132:133], v[132:133], v[136:137] neg_lo:[0,1] neg_hi:[0,1]
	v_cmp_neq_f32_e32 vcc, s39, v144
	v_add_f32_e32 v133, v140, v133
	v_add_f32_e32 v132, v132, v133
	v_add_f32_e32 v133, v135, v132
	v_mul_f32_e32 v137, v139, v133
	v_mul_f32_e32 v134, v138, v137
	v_sub_f32_e32 v135, v135, v133
	v_add_f32_e32 v142, v141, v137
	v_fma_f32 v136, v137, v138, -v134
	v_add_f32_e32 v140, v132, v135
	v_sub_f32_e32 v132, v142, v141
	v_fmac_f32_e32 v136, v137, v131
	v_sub_f32_e32 v131, v137, v132
	v_add_f32_e32 v132, v134, v136
	v_sub_f32_e32 v135, v133, v132
	v_mov_b32_e32 v137, v132
	v_pk_add_f32 v[132:133], v[132:133], v[134:135] neg_lo:[0,1] neg_hi:[0,1]
	v_lshl_add_u64 v[128:129], v[128:129], 0, v[204:205]
	v_pk_add_f32 v[132:133], v[132:133], v[136:137] neg_lo:[0,1] neg_hi:[0,1]
	v_mov_b32_e32 v136, 0x3ecc95a3
	v_add_f32_e32 v133, v140, v133
	v_add_f32_e32 v132, v132, v133
	v_add_f32_e32 v132, v135, v132
	v_mul_f32_e32 v132, v139, v132
	v_add_f32_e32 v131, v131, v132
	v_add_f32_e32 v132, v142, v131
	v_mul_f32_e32 v134, v132, v132
	v_sub_f32_e32 v135, v132, v142
	v_fmamk_f32 v136, v134, 0x3e9b6dac, v136
	v_sub_f32_e32 v135, v131, v135
	v_mul_f32_e32 v131, v132, v134
	v_fmaak_f32 v207, v134, v136, 0x3f2aaada
	v_ldexp_f32 v137, v135, 1
	v_pk_mul_f32 v[134:135], v[130:131], v[206:207]
	v_ldexp_f32 v133, v132, 1
	v_fma_f32 v132, v130, s38, -v134
	v_fmac_f32_e32 v132, 0xb102e308, v130
	v_pk_add_f32 v[130:131], v[134:135], v[132:133]
	v_mov_b32_e32 v136, v134
	v_sub_f32_e32 v140, v131, v133
	v_pk_add_f32 v[138:139], v[130:131], v[134:135] neg_lo:[0,1] neg_hi:[0,1]
	v_sub_f32_e32 v134, v135, v140
	v_add_f32_e32 v137, v137, v134
	v_pk_add_f32 v[134:135], v[130:131], v[136:137]
	v_mov_b32_e32 v133, v130
	v_mov_b32_e32 v139, v135
	v_pk_add_f32 v[142:143], v[132:133], v[138:139] neg_lo:[0,1] neg_hi:[0,1]
	v_pk_add_f32 v[132:133], v[132:133], v[138:139]
	v_mov_b32_e32 v141, v130
	v_pk_add_f32 v[138:139], v[132:133], v[130:131] op_sel:[1,0] op_sel_hi:[0,1] neg_lo:[0,1] neg_hi:[0,1]
	v_mov_b32_e32 v140, v137
	v_mov_b32_e32 v136, v135
	v_mov_b32_e32 v137, v133
	v_pk_mov_b32 v[130:131], v[130:131], v[138:139] op_sel:[1,0]
	v_pk_add_f32 v[134:135], v[134:135], v[138:139] op_sel_hi:[1,0] neg_lo:[0,1] neg_hi:[0,1]
	v_pk_add_f32 v[130:131], v[136:137], v[130:131] neg_lo:[0,1] neg_hi:[0,1]
	v_mov_b32_e32 v134, v142
	v_pk_add_f32 v[130:131], v[140:141], v[130:131] neg_lo:[0,1] neg_hi:[0,1]
	v_mov_b32_e32 v143, v133
	v_pk_add_f32 v[134:135], v[134:135], v[130:131]
	s_nop 0
	v_pk_add_f32 v[136:137], v[134:135], v[134:135] op_sel:[0,1] op_sel_hi:[1,0]
	s_nop 0
	v_pk_add_f32 v[132:133], v[132:133], v[136:137] op_sel:[1,0] op_sel_hi:[0,1]
	v_mov_b32_e32 v135, v132
	v_mov_b32_e32 v131, v136
	v_pk_add_f32 v[136:137], v[134:135], v[142:143] neg_lo:[0,1] neg_hi:[0,1]
	s_nop 0
	v_sub_f32_e32 v133, v134, v136
	v_pk_add_f32 v[130:131], v[130:131], v[136:137] neg_lo:[0,1] neg_hi:[0,1]
	v_sub_f32_e32 v133, v142, v133
	v_add_f32_e32 v130, v130, v133
	v_add_f32_e32 v130, v130, v131
	v_add_f32_e32 v130, v132, v130
	v_mov_b32_e32 v131, 0x7f800000
	v_cndmask_b32_e32 v130, v131, v130, vcc
	v_cmp_ngt_f32_e32 vcc, -1.0, v144
	v_mov_b32_e32 v131, 0x7fc00000
	s_nop 0
	v_cndmask_b32_e32 v130, v131, v130, vcc
	v_cmp_neq_f32_e32 vcc, -1.0, v144
	v_mov_b32_e32 v131, 0xff800000
	s_nop 0
	v_cndmask_b32_e32 v130, v131, v130, vcc
	v_cmp_lt_f32_e64 vcc, |v144|, s40
	s_nop 1
	v_cndmask_b32_e32 v130, v130, v144, vcc
	v_sub_f32_e32 v130, v145, v130
	global_store_dword v[128:129], v130, off
	s_branch .LBB0_152
